# P6: the two interleaved LayerNorm wave sums also use the DPP + permlane all-reduce (later butterfly steps become copies)
# baseline (speedup 1.0000x reference)
.LBB0_986:
	v_mov_b32_e32 v246, v191
	v_mov_b32_e32 v247, v192
	v_mov_b32_e32 v248, v190
	v_mov_b32_e32 v249, v193
	v_pk_add_f32 v[246:247], v[246:247], v[248:249]
	v_mov_b32_e32 v248, v187
	v_mov_b32_e32 v249, v188
	v_mov_b32_e32 v216, v186
	v_mov_b32_e32 v217, v189
	v_pk_add_f32 v[216:217], v[248:249], v[216:217]
	v_add_f32_e32 v209, v246, v247
	v_pk_add_f32 v[216:217], v[216:217], v[216:217] op_sel:[0,1] op_sel_hi:[1,0]
	v_add_f32_e32 v246, 0, v209
	v_add_f32_e32 v248, v182, v183
	v_add_f32_e32 v218, v184, v185
	v_mov_b32_e32 v247, v178
	v_mov_b32_e32 v217, v179
	v_mov_b32_e32 v249, v180
	v_mov_b32_e32 v219, v181
	v_pk_add_f32 v[216:217], v[246:247], v[216:217]
	v_pk_add_f32 v[218:219], v[248:249], v[218:219]
	s_mov_b32 s36, 0xf800000
	v_pk_add_f32 v[216:217], v[216:217], v[218:219]
	s_nop 0
	v_add_f32_e32 v209, v216, v217
	s_nop 1
	v_add_f32_dpp v209, v209, v209 quad_perm:[1,0,3,2] row_mask:0xf bank_mask:0xf
	s_nop 1
	v_add_f32_dpp v209, v209, v209 quad_perm:[2,3,0,1] row_mask:0xf bank_mask:0xf
	s_nop 1
	v_add_f32_dpp v209, v209, v209 row_half_mirror row_mask:0xf bank_mask:0xf
	s_nop 1
	v_add_f32_dpp v209, v209, v209 row_mirror row_mask:0xf bank_mask:0xf
	v_mov_b32_e32 v216, v209
	s_nop 1
	v_permlane16_swap_b32_e32 v216, v209
	s_nop 1
	v_add_f32_e32 v209, v209, v216
	v_mov_b32_e32 v216, v209
	s_nop 1
	v_permlane32_swap_b32_e32 v216, v209
	s_nop 1
	v_add_f32_e32 v209, v209, v216
	v_fmamk_f32 v191, v209, 0xba800000, v191
	v_fmamk_f32 v190, v209, 0xba800000, v190
	v_fmamk_f32 v193, v209, 0xba800000, v193
	v_fmac_f32_e32 v192, 0xba800000, v209
	v_pk_mul_f32 v[216:217], v[192:193], v[192:193]
	v_pk_mul_f32 v[218:219], v[190:191], v[190:191]
	v_fmamk_f32 v187, v209, 0xba800000, v187
	v_fmamk_f32 v186, v209, 0xba800000, v186
	v_fmamk_f32 v189, v209, 0xba800000, v189
	v_pk_mov_b32 v[246:247], v[218:219], v[216:217] op_sel:[1,0]
	v_mov_b32_e32 v219, v217
	v_fmac_f32_e32 v188, 0xba800000, v209
	v_pk_add_f32 v[216:217], v[246:247], v[218:219]
	v_pk_mul_f32 v[218:219], v[188:189], v[188:189]
	v_pk_mul_f32 v[246:247], v[186:187], v[186:187]
	v_fmac_f32_e32 v184, 0xba800000, v209
	v_pk_mov_b32 v[248:249], v[246:247], v[218:219] op_sel:[1,0]
	v_mov_b32_e32 v247, v219
	v_pk_add_f32 v[218:219], v[248:249], v[246:247]
	v_fmamk_f32 v246, v209, 0xba800000, v182
	v_fmamk_f32 v247, v209, 0xba800000, v183
	v_mul_f32_e32 v182, v246, v246
	v_pk_fma_f32 v[182:183], v[246:247], v[246:247], v[182:183] op_sel_hi:[1,1,0]
	v_fmamk_f32 v185, v209, 0xba800000, v185
	v_mul_f32_e32 v182, v184, v184
	v_pk_add_f32 v[216:217], v[216:217], v[216:217] op_sel_hi:[0,1]
	v_pk_add_f32 v[218:219], v[218:219], v[218:219] op_sel_hi:[0,1]
	v_pk_fma_f32 v[248:249], v[184:185], v[184:185], v[182:183] op_sel_hi:[1,1,0]
	v_fmamk_f32 v181, v209, 0xba800000, v181
	v_fmamk_f32 v180, v209, 0xba800000, v180
	v_fmamk_f32 v179, v209, 0xba800000, v179
	v_fmac_f32_e32 v178, 0xba800000, v209
	v_mul_f32_e32 v182, v178, v178
	v_mul_f32_e32 v248, v179, v179
	v_mul_f32_e32 v216, v180, v180
	v_mul_f32_e32 v218, v181, v181
	v_pk_add_f32 v[182:183], v[182:183], v[248:249]
	v_pk_add_f32 v[216:217], v[216:217], v[218:219]
	s_nop 0
	v_pk_add_f32 v[182:183], v[182:183], v[216:217]
	s_nop 0
	v_add_f32_e32 v182, v182, v183
	s_nop 1
	v_add_f32_dpp v182, v182, v182 quad_perm:[1,0,3,2] row_mask:0xf bank_mask:0xf
	s_nop 1
	v_add_f32_dpp v182, v182, v182 quad_perm:[2,3,0,1] row_mask:0xf bank_mask:0xf
	s_nop 1
	v_add_f32_dpp v182, v182, v182 row_half_mirror row_mask:0xf bank_mask:0xf
	s_nop 1
	v_add_f32_dpp v182, v182, v182 row_mirror row_mask:0xf bank_mask:0xf
	v_mov_b32_e32 v183, v182
	s_nop 1
	v_permlane16_swap_b32_e32 v183, v182
	s_nop 1
	v_add_f32_e32 v182, v182, v183
	v_mov_b32_e32 v183, v182
	s_nop 1
	v_permlane32_swap_b32_e32 v183, v182
	s_nop 1
	v_add_f32_e32 v182, v182, v183
	v_fmamk_f32 v182, v182, 0x3a800000, v211
	v_mul_f32_e32 v183, 0x4f800000, v182
	v_cmp_gt_f32_e32 vcc, s36, v182
	s_nop 1
	v_cndmask_b32_e32 v182, v182, v183, vcc
	v_sqrt_f32_e32 v183, v182
	s_nop 0
	v_add_u32_e32 v209, -1, v183
	v_add_u32_e32 v216, 1, v183
	v_fma_f32 v217, -v209, v183, v182
	v_fma_f32 v218, -v216, v183, v182
	v_cmp_ge_f32_e64 s[12:13], 0, v217
	s_nop 1
	v_cndmask_b32_e64 v183, v183, v209, s[12:13]
	v_cmp_lt_f32_e64 s[12:13], 0, v218
	s_nop 1
	v_cndmask_b32_e64 v183, v183, v216, s[12:13]
	v_mul_f32_e32 v209, 0x37800000, v183
	v_cndmask_b32_e32 v183, v183, v209, vcc
	v_cmp_class_f32_e32 vcc, v182, v212
	s_nop 1
	v_cndmask_b32_e32 v182, v183, v182, vcc
	v_div_scale_f32 v183, s[12:13], v182, v182, 1.0
	v_rcp_f32_e32 v209, v183
	v_readlane_b32 s12, v252, 4
	s_add_i32 s34, s12, s14
	s_ashr_i32 s35, s34, 31
	v_fma_f32 v216, -v183, v209, 1.0
	v_fmac_f32_e32 v209, v216, v209
	v_div_scale_f32 v216, vcc, 1.0, v182, 1.0
	v_mul_f32_e32 v217, v216, v209
	v_fma_f32 v218, -v183, v217, v216
	v_fmac_f32_e32 v217, v218, v209
	v_fma_f32 v183, -v183, v217, v216
	v_div_fmas_f32 v183, v183, v209, v217
	v_div_fixup_f32 v182, v183, v182, 1.0
	v_pk_mul_f32 v[190:191], v[190:191], v[182:183] op_sel_hi:[1,0]
	s_lshl_b64 s[12:13], s[34:35], 10
	s_waitcnt vmcnt(22)
	v_pk_fma_f32 v[190:191], v[2:3], v[190:191], v[6:7]
	v_pk_mul_f32 v[192:193], v[192:193], v[182:183] op_sel_hi:[1,0]
	v_pk_fma_f32 v[190:191], v[98:99], v[190:191], v[118:119]
	s_mov_b32 s35, 0xffff
	v_cvt_pk_bf16_f32 v216, v191, 0
	v_cvt_pk_bf16_f32 v183, v190, 0
	v_lshlrev_b32_e32 v216, 16, v216
	v_lshlrev_b32_e32 v209, 16, v183
	v_sub_f32_e32 v217, v191, v216
	v_and_or_b32 v216, v183, s35, v216
	v_mov_b32_e32 v183, v1
	v_cvt_pk_fp8_f32 v183, v190, v191
	v_pk_fma_f32 v[192:193], v[4:5], v[192:193], v[8:9]
	v_cvt_pk_bf16_f32 v218, v217, 0
	v_pk_fma_f32 v[192:193], v[100:101], v[192:193], v[120:121]
	v_sub_f32_e32 v209, v190, v209
	v_cvt_pk_fp8_f32 v183, v192, v193 op_sel:[0,0,1]
	v_cvt_pk_bf16_f32 v217, v192, 0
	v_cvt_pk_bf16_f32 v248, v193, 0
	v_lshlrev_b32_e32 v219, 16, v217
	v_lshlrev_b32_e32 v248, 16, v248
	v_sub_f32_e32 v219, v192, v219
	v_sub_f32_e32 v249, v193, v248
	v_lshl_add_u64 v[192:193], v[202:203], 0, s[12:13]
	global_store_dword v[192:193], v183, off
	v_add_u32_e32 v183, s47, v234
	v_pk_mul_f32 v[186:187], v[186:187], v[182:183] op_sel_hi:[1,0]
	v_cvt_pk_bf16_f32 v249, v249, 0
	s_waitcnt vmcnt(20)
	v_pk_fma_f32 v[186:187], v[10:11], v[186:187], v[18:19]
	v_cvt_pk_bf16_f32 v209, v209, 0
	v_cvt_pk_bf16_f32 v219, v219, 0
	v_and_or_b32 v217, v217, s35, v248
	v_lshlrev_b32_e32 v190, 16, v218
	v_lshlrev_b32_e32 v191, 16, v249
	v_pk_fma_f32 v[186:187], v[138:139], v[186:187], v[142:143]
	v_and_or_b32 v190, v209, s35, v190
	v_and_or_b32 v191, v219, s35, v191
	ds_write_b64 v183, v[216:217]
	ds_write_b64 v183, v[190:191] offset:33024
	v_pk_mul_f32 v[188:189], v[188:189], v[182:183] op_sel_hi:[1,0]
	v_cvt_pk_bf16_f32 v183, v186, 0
	v_lshlrev_b32_e32 v190, 16, v183
	v_sub_f32_e32 v190, v186, v190
	v_cvt_pk_bf16_f32 v192, v190, 0
	v_cvt_pk_bf16_f32 v190, v187, 0
	v_lshlrev_b32_e32 v190, 16, v190
	v_sub_f32_e32 v191, v187, v190
	v_cvt_pk_bf16_f32 v193, v191, 0
	v_and_or_b32 v190, v183, s35, v190
	v_lshlrev_b32_e32 v183, 16, v193
	v_mov_b32_e32 v193, v1
	v_pk_fma_f32 v[188:189], v[12:13], v[188:189], v[20:21]
	v_cvt_pk_fp8_f32 v193, v186, v187
	v_pk_fma_f32 v[188:189], v[140:141], v[188:189], v[144:145]
	s_add_u32 s12, s20, s12
	v_cvt_pk_bf16_f32 v216, v189, 0
	v_cvt_pk_bf16_f32 v191, v188, 0
	v_lshlrev_b32_e32 v216, 16, v216
	v_lshlrev_b32_e32 v209, 16, v191
	v_sub_f32_e32 v217, v189, v216
	v_cvt_pk_fp8_f32 v193, v188, v189 op_sel:[0,0,1]
	v_sub_f32_e32 v209, v188, v209
	v_cvt_pk_bf16_f32 v217, v217, 0
	v_cvt_pk_bf16_f32 v209, v209, 0
	v_and_or_b32 v186, v192, s35, v183
	v_lshlrev_b32_e32 v183, 16, v217
	s_addc_u32 s13, s21, s13
	v_and_or_b32 v191, v191, s35, v216
	v_and_or_b32 v187, v209, s35, v183
	v_lshl_add_u64 v[188:189], s[12:13], 0, v[0:1]
	v_add_u32_e32 v183, s47, v235
	global_store_dword v[188:189], v193, off
	ds_write_b64 v183, v[190:191]
	ds_write_b64 v183, v[186:187] offset:33024
	v_pk_mul_f32 v[186:187], v[246:247], v[182:183] op_sel_hi:[1,0]
	v_pk_mul_f32 v[184:185], v[184:185], v[182:183] op_sel_hi:[1,0]
	s_waitcnt vmcnt(20)
	v_pk_fma_f32 v[186:187], v[14:15], v[186:187], v[22:23]
	v_pk_fma_f32 v[184:185], v[16:17], v[184:185], v[24:25]
	v_pk_fma_f32 v[186:187], v[150:151], v[186:187], v[146:147]
	v_pk_fma_f32 v[184:185], v[152:153], v[184:185], v[148:149]
	v_cvt_pk_bf16_f32 v183, v186, 0
	v_lshlrev_b32_e32 v188, 16, v183
	v_sub_f32_e32 v188, v186, v188
	v_cvt_pk_bf16_f32 v209, v188, 0
	v_cvt_pk_bf16_f32 v188, v187, 0
	v_lshlrev_b32_e32 v218, 16, v188
	v_sub_f32_e32 v188, v187, v218
	v_cvt_pk_bf16_f32 v246, v184, 0
	v_cvt_pk_bf16_f32 v219, v188, 0
	v_lshlrev_b32_e32 v188, 16, v246
	v_sub_f32_e32 v188, v184, v188
	v_cvt_pk_bf16_f32 v247, v188, 0
	v_mov_b32_e32 v188, v175
	v_mov_b32_e32 v189, v176
	v_mov_b32_e32 v190, v174
	v_mov_b32_e32 v191, v177
	v_pk_add_f32 v[188:189], v[188:189], v[190:191]
	v_mov_b32_e32 v190, v171
	v_mov_b32_e32 v191, v172
	v_mov_b32_e32 v192, v170
	v_mov_b32_e32 v193, v173
	v_pk_add_f32 v[190:191], v[190:191], v[192:193]
	v_add_f32_e32 v188, v188, v189
	v_pk_add_f32 v[190:191], v[190:191], v[190:191] op_sel:[0,1] op_sel_hi:[1,0]
	v_add_f32_e32 v188, 0, v188
	v_add_f32_e32 v192, v166, v167
	v_add_f32_e32 v216, v168, v169
	v_mov_b32_e32 v189, v162
	v_mov_b32_e32 v191, v163
	v_mov_b32_e32 v193, v164
	v_mov_b32_e32 v217, v165
	v_pk_add_f32 v[188:189], v[188:189], v[190:191]
	v_pk_add_f32 v[190:191], v[192:193], v[216:217]
	v_cvt_pk_bf16_f32 v248, v185, 0
	v_pk_add_f32 v[188:189], v[188:189], v[190:191]
	v_lshlrev_b32_e32 v191, 16, v248
	v_add_f32_e32 v189, v188, v189
	s_nop 1
	v_add_f32_dpp v189, v189, v189 quad_perm:[1,0,3,2] row_mask:0xf bank_mask:0xf
	s_nop 1
	v_add_f32_dpp v189, v189, v189 quad_perm:[2,3,0,1] row_mask:0xf bank_mask:0xf
	s_nop 1
	v_add_f32_dpp v189, v189, v189 row_half_mirror row_mask:0xf bank_mask:0xf
	s_nop 1
	v_add_f32_dpp v189, v189, v189 row_mirror row_mask:0xf bank_mask:0xf
	v_mov_b32_e32 v190, v189
	s_nop 1
	v_permlane16_swap_b32_e32 v190, v189
	s_nop 1
	v_add_f32_e32 v189, v189, v190
	v_mov_b32_e32 v190, v189
	s_nop 1
	v_permlane32_swap_b32_e32 v190, v189
	s_nop 1
	v_add_f32_e32 v189, v189, v190
	v_sub_f32_e32 v188, v185, v191
	v_cvt_pk_bf16_f32 v192, v188, 0
	v_and_or_b32 v188, v183, s35, v218
	v_mov_b32_e32 v193, v1
	s_waitcnt lgkmcnt(0)
	v_mov_b32_e32 v183, v189
	v_cvt_pk_fp8_f32 v193, v186, v187
	v_and_or_b32 v189, v246, s35, v191
	v_lshlrev_b32_e32 v191, 16, v219
	v_and_or_b32 v186, v209, s35, v191
	s_waitcnt lgkmcnt(0)
	v_cvt_pk_fp8_f32 v193, v184, v185 op_sel:[0,0,1]
	v_lshl_add_u64 v[184:185], s[12:13], 0, v[198:199]
	v_lshlrev_b32_e32 v187, 16, v192
	v_and_or_b32 v187, v247, s35, v187
	s_waitcnt lgkmcnt(0)
	global_store_dword v[184:185], v193, off
	v_add_u32_e32 v184, s47, v236
	ds_write_b64 v184, v[188:189]
	ds_write_b64 v184, v[186:187] offset:33024
	s_waitcnt lgkmcnt(2)
	v_pk_mul_f32 v[180:181], v[180:181], v[182:183] op_sel_hi:[1,0]
	v_pk_mul_f32 v[178:179], v[178:179], v[182:183] op_sel_hi:[1,0]
	s_waitcnt vmcnt(19)
	v_pk_fma_f32 v[180:181], v[28:29], v[180:181], v[32:33]
	v_pk_fma_f32 v[178:179], v[26:27], v[178:179], v[30:31]
	s_waitcnt lgkmcnt(0)
	v_mov_b32_e32 v182, v183
	s_waitcnt vmcnt(3)
	v_pk_fma_f32 v[180:181], v[156:157], v[180:181], v[160:161]
	v_pk_fma_f32 v[178:179], v[154:155], v[178:179], v[158:159]
	s_waitcnt lgkmcnt(0)
	v_mov_b32_e32 v191, v182
	v_fmamk_f32 v175, v191, 0xba800000, v175
	v_fmamk_f32 v174, v191, 0xba800000, v174
	v_fmamk_f32 v177, v191, 0xba800000, v177
	v_fmac_f32_e32 v176, 0xba800000, v191
	v_pk_mul_f32 v[182:183], v[176:177], v[176:177]
	v_pk_mul_f32 v[184:185], v[174:175], v[174:175]
	v_fmamk_f32 v171, v191, 0xba800000, v171
	v_pk_mov_b32 v[186:187], v[184:185], v[182:183] op_sel:[1,0]
	v_mov_b32_e32 v185, v183
	v_pk_add_f32 v[182:183], v[186:187], v[184:185]
	v_fmamk_f32 v170, v191, 0xba800000, v170
	v_fmamk_f32 v173, v191, 0xba800000, v173
	v_fmac_f32_e32 v172, 0xba800000, v191
	v_pk_add_f32 v[182:183], v[182:183], v[182:183] op_sel_hi:[0,1]
	v_pk_mul_f32 v[184:185], v[172:173], v[172:173]
	v_pk_mul_f32 v[186:187], v[170:171], v[170:171]
	v_fmamk_f32 v166, v191, 0xba800000, v166
	v_pk_mov_b32 v[188:189], v[186:187], v[184:185] op_sel:[1,0]
	v_mov_b32_e32 v187, v185
	v_fmamk_f32 v167, v191, 0xba800000, v167
	v_fmac_f32_e32 v168, 0xba800000, v191
	v_mul_f32_e32 v182, v166, v166
	v_pk_add_f32 v[184:185], v[188:189], v[186:187]
	v_fmamk_f32 v169, v191, 0xba800000, v169
	v_pk_fma_f32 v[186:187], v[166:167], v[166:167], v[182:183] op_sel_hi:[1,1,0]
	v_mul_f32_e32 v182, v168, v168
	v_pk_add_f32 v[184:185], v[184:185], v[184:185] op_sel_hi:[0,1]
	v_pk_fma_f32 v[188:189], v[168:169], v[168:169], v[182:183] op_sel_hi:[1,1,0]
	v_fmamk_f32 v165, v191, 0xba800000, v165
	v_fmamk_f32 v164, v191, 0xba800000, v164
	v_fmamk_f32 v163, v191, 0xba800000, v163
	v_fmac_f32_e32 v162, 0xba800000, v191
	v_mul_f32_e32 v186, v162, v162
	v_mul_f32_e32 v188, v163, v163
	v_mul_f32_e32 v182, v164, v164
	v_mul_f32_e32 v184, v165, v165
	v_pk_add_f32 v[186:187], v[186:187], v[188:189]
	v_pk_add_f32 v[182:183], v[182:183], v[184:185]
	v_cvt_pk_bf16_f32 v189, v181, 0
	v_pk_add_f32 v[182:183], v[186:187], v[182:183]
	v_cvt_pk_bf16_f32 v185, v179, 0
	v_add_f32_e32 v182, v182, v183
	s_nop 1
	v_add_f32_dpp v182, v182, v182 quad_perm:[1,0,3,2] row_mask:0xf bank_mask:0xf
	s_nop 1
	v_add_f32_dpp v182, v182, v182 quad_perm:[2,3,0,1] row_mask:0xf bank_mask:0xf
	s_nop 1
	v_add_f32_dpp v182, v182, v182 row_half_mirror row_mask:0xf bank_mask:0xf
	s_nop 1
	v_add_f32_dpp v182, v182, v182 row_mirror row_mask:0xf bank_mask:0xf
	v_mov_b32_e32 v183, v182
	s_nop 1
	v_permlane16_swap_b32_e32 v183, v182
	s_nop 1
	v_add_f32_e32 v182, v182, v183
	v_mov_b32_e32 v183, v182
	s_nop 1
	v_permlane32_swap_b32_e32 v183, v182
	s_nop 1
	v_add_f32_e32 v182, v182, v183
	v_lshlrev_b32_e32 v189, 16, v189
	v_cvt_pk_bf16_f32 v190, v178, 0
	v_lshlrev_b32_e32 v185, 16, v185
	v_sub_f32_e32 v186, v179, v185
	s_waitcnt lgkmcnt(0)
	v_lshlrev_b32_e32 v184, 16, v190
	v_cvt_pk_bf16_f32 v187, v180, 0
	v_lshlrev_b32_e32 v188, 16, v187
	v_sub_f32_e32 v188, v180, v188
	s_waitcnt lgkmcnt(0)
	v_sub_f32_e32 v184, v178, v184
	v_cvt_pk_bf16_f32 v186, v186, 0
	v_cvt_pk_bf16_f32 v184, v184, 0
	v_lshlrev_b32_e32 v186, 16, v186
	s_waitcnt lgkmcnt(0)
	v_mov_b32_e32 v183, v182
	v_sub_f32_e32 v182, v181, v189
	v_cvt_pk_bf16_f32 v192, v182, 0
	v_and_or_b32 v182, v190, s35, v185
	v_cvt_pk_bf16_f32 v188, v188, 0
	s_waitcnt lgkmcnt(0)
	v_mov_b32_e32 v185, v183
	v_and_or_b32 v183, v187, s35, v189
	v_mov_b32_e32 v187, v1
	v_cvt_pk_fp8_f32 v187, v178, v179
	v_and_or_b32 v178, v184, s35, v186
	s_waitcnt lgkmcnt(0)
	v_cvt_pk_fp8_f32 v187, v180, v181 op_sel:[0,0,1]
	v_lshlrev_b32_e32 v179, 16, v192
	v_and_or_b32 v179, v188, s35, v179
	s_waitcnt lgkmcnt(0)
	v_mov_b32_e32 v180, v185
	v_fmamk_f32 v180, v180, 0x3a800000, v211
	v_mul_f32_e32 v181, 0x4f800000, v180
	v_cmp_gt_f32_e32 vcc, s36, v180
	s_nop 1
	v_cndmask_b32_e32 v184, v180, v181, vcc
	v_sqrt_f32_e32 v185, v184
	v_lshl_add_u64 v[180:181], s[12:13], 0, v[200:201]
	global_store_dword v[180:181], v187, off
	v_add_u32_e32 v180, s47, v237
	v_add_u32_e32 v181, -1, v185
	v_fma_f32 v186, -v181, v185, v184
	v_cmp_ge_f32_e64 s[12:13], 0, v186
	v_add_u32_e32 v186, 1, v185
	ds_write_b64 v180, v[182:183]
	ds_write_b64 v180, v[178:179] offset:33024
	v_cndmask_b32_e64 v181, v185, v181, s[12:13]
	v_fma_f32 v185, -v186, v185, v184
	v_cmp_lt_f32_e64 s[12:13], 0, v185
	s_nop 1
	v_cndmask_b32_e64 v181, v181, v186, s[12:13]
	v_mul_f32_e32 v185, 0x37800000, v181
	v_cndmask_b32_e32 v181, v181, v185, vcc
	v_cmp_class_f32_e32 vcc, v184, v212
	s_nop 1
	v_cndmask_b32_e32 v181, v181, v184, vcc
	v_div_scale_f32 v184, s[12:13], v181, v181, 1.0
	v_rcp_f32_e32 v185, v184
	s_add_i32 s12, s34, 1
	s_ashr_i32 s13, s12, 31
	s_lshl_b64 s[12:13], s[12:13], 10
	v_fma_f32 v178, -v184, v185, 1.0
	v_fmac_f32_e32 v185, v178, v185
	v_div_scale_f32 v178, vcc, 1.0, v181, 1.0
	v_mul_f32_e32 v179, v178, v185
	v_fma_f32 v180, -v184, v179, v178
	v_fmac_f32_e32 v179, v180, v185
	v_fma_f32 v178, -v184, v179, v178
	v_div_fmas_f32 v178, v178, v185, v179
	v_div_fixup_f32 v178, v178, v181, 1.0
	v_pk_mul_f32 v[174:175], v[174:175], v[178:179] op_sel_hi:[1,0]
	v_pk_mul_f32 v[176:177], v[176:177], v[178:179] op_sel_hi:[1,0]
	v_pk_fma_f32 v[174:175], v[2:3], v[174:175], v[6:7]
	v_pk_fma_f32 v[176:177], v[4:5], v[176:177], v[8:9]
	v_pk_fma_f32 v[174:175], v[98:99], v[174:175], v[118:119]
	v_pk_fma_f32 v[176:177], v[100:101], v[176:177], v[120:121]
	v_cvt_pk_bf16_f32 v179, v174, 0
	v_lshlrev_b32_e32 v180, 16, v179
	v_sub_f32_e32 v180, v174, v180
	v_cvt_pk_bf16_f32 v182, v180, 0
	v_cvt_pk_bf16_f32 v180, v175, 0
	v_lshlrev_b32_e32 v180, 16, v180
	v_sub_f32_e32 v181, v175, v180
	v_and_or_b32 v180, v179, s35, v180
	v_mov_b32_e32 v179, v1
	v_cvt_pk_fp8_f32 v179, v174, v175
	v_cvt_pk_bf16_f32 v185, v177, 0
	v_cvt_pk_bf16_f32 v183, v181, 0
	v_cvt_pk_bf16_f32 v181, v176, 0
	v_cvt_pk_fp8_f32 v179, v176, v177 op_sel:[0,0,1]
	v_lshlrev_b32_e32 v185, 16, v185
	v_lshlrev_b32_e32 v184, 16, v181
	v_sub_f32_e32 v186, v177, v185
	v_pk_mul_f32 v[170:171], v[170:171], v[178:179] op_sel_hi:[1,0]
	v_sub_f32_e32 v184, v176, v184
	v_cvt_pk_bf16_f32 v186, v186, 0
	v_lshlrev_b32_e32 v174, 16, v183
	v_lshl_add_u64 v[176:177], v[202:203], 0, s[12:13]
	v_pk_fma_f32 v[170:171], v[10:11], v[170:171], v[18:19]
	v_cvt_pk_bf16_f32 v184, v184, 0
	v_and_or_b32 v181, v181, s35, v185
	v_and_or_b32 v174, v182, s35, v174
	v_lshlrev_b32_e32 v175, 16, v186
	global_store_dword v[176:177], v179, off
	v_add_u32_e32 v176, s48, v234
	v_pk_fma_f32 v[170:171], v[138:139], v[170:171], v[142:143]
	v_and_or_b32 v175, v184, s35, v175
	ds_write_b64 v176, v[180:181]
	ds_write_b64 v176, v[174:175] offset:33024
	v_pk_mul_f32 v[172:173], v[172:173], v[178:179] op_sel_hi:[1,0]
	v_cvt_pk_bf16_f32 v174, v170, 0
	v_pk_fma_f32 v[172:173], v[12:13], v[172:173], v[20:21]
	v_lshlrev_b32_e32 v175, 16, v174
	v_pk_fma_f32 v[172:173], v[140:141], v[172:173], v[144:145]
	v_sub_f32_e32 v175, v170, v175
	v_cvt_pk_bf16_f32 v176, v175, 0
	v_cvt_pk_bf16_f32 v175, v171, 0
	v_cvt_pk_bf16_f32 v181, v173, 0
	v_lshlrev_b32_e32 v175, 16, v175
	v_cvt_pk_bf16_f32 v179, v172, 0
	v_lshlrev_b32_e32 v181, 16, v181
	v_sub_f32_e32 v177, v171, v175
	v_lshlrev_b32_e32 v180, 16, v179
	v_and_or_b32 v174, v174, s35, v175
	v_and_or_b32 v175, v179, s35, v181
	v_mov_b32_e32 v179, v1
	v_cvt_pk_fp8_f32 v179, v170, v171
	s_add_u32 s12, s20, s12
	s_addc_u32 s13, s21, s13
	v_sub_f32_e32 v180, v172, v180
	v_cvt_pk_fp8_f32 v179, v172, v173 op_sel:[0,0,1]
	v_sub_f32_e32 v182, v173, v181
	v_lshl_add_u64 v[172:173], s[12:13], 0, v[0:1]
	v_cvt_pk_bf16_f32 v177, v177, 0
	v_pk_mul_f32 v[166:167], v[166:167], v[178:179] op_sel_hi:[1,0]
	global_store_dword v[172:173], v179, off
	v_pk_fma_f32 v[166:167], v[14:15], v[166:167], v[22:23]
	v_pk_mul_f32 v[168:169], v[168:169], v[178:179] op_sel_hi:[1,0]
	v_pk_fma_f32 v[166:167], v[150:151], v[166:167], v[146:147]
	v_mov_b32_e32 v179, v1
	v_cvt_pk_bf16_f32 v182, v182, 0
	v_lshlrev_b32_e32 v177, 16, v177
	v_cvt_pk_fp8_f32 v179, v166, v167
	v_cvt_pk_bf16_f32 v180, v180, 0
	v_and_or_b32 v170, v176, s35, v177
	v_lshlrev_b32_e32 v171, 16, v182
	v_add_u32_e32 v172, s48, v235
	v_and_or_b32 v171, v180, s35, v171
	ds_write_b64 v172, v[174:175]
	ds_write_b64 v172, v[170:171] offset:33024
	v_pk_fma_f32 v[168:169], v[16:17], v[168:169], v[24:25]
	v_cvt_pk_bf16_f32 v170, v166, 0
	v_pk_fma_f32 v[168:169], v[152:153], v[168:169], v[148:149]
	v_lshlrev_b32_e32 v171, 16, v170
	v_sub_f32_e32 v171, v166, v171
	v_cvt_pk_fp8_f32 v179, v168, v169 op_sel:[0,0,1]
	v_cvt_pk_bf16_f32 v172, v171, 0
	v_cvt_pk_bf16_f32 v171, v167, 0
	v_lshlrev_b32_e32 v171, 16, v171
	v_cvt_pk_bf16_f32 v176, v169, 0
	v_sub_f32_e32 v173, v167, v171
	v_cvt_pk_bf16_f32 v174, v168, 0
	v_lshlrev_b32_e32 v176, 16, v176
	v_cvt_pk_bf16_f32 v173, v173, 0
	v_lshlrev_b32_e32 v175, 16, v174
	v_sub_f32_e32 v177, v169, v176
	v_pk_mul_f32 v[162:163], v[162:163], v[178:179] op_sel_hi:[1,0]
	v_sub_f32_e32 v175, v168, v175
	v_cvt_pk_bf16_f32 v177, v177, 0
	v_lshlrev_b32_e32 v166, 16, v173
	v_lshl_add_u64 v[168:169], s[12:13], 0, v[198:199]
	v_pk_fma_f32 v[162:163], v[26:27], v[162:163], v[30:31]
	v_cvt_pk_bf16_f32 v175, v175, 0
	v_and_or_b32 v170, v170, s35, v171
	v_and_or_b32 v171, v174, s35, v176
	v_and_or_b32 v166, v172, s35, v166
	v_lshlrev_b32_e32 v167, 16, v177
	global_store_dword v[168:169], v179, off
	v_add_u32_e32 v168, s48, v236
	v_pk_fma_f32 v[162:163], v[154:155], v[162:163], v[158:159]
	v_mov_b32_e32 v174, v1
	v_and_or_b32 v167, v175, s35, v167
	ds_write_b64 v168, v[170:171]
	ds_write_b64 v168, v[166:167] offset:33024
	v_pk_mul_f32 v[164:165], v[164:165], v[178:179] op_sel_hi:[1,0]
	v_cvt_pk_bf16_f32 v166, v162, 0
	v_cvt_pk_fp8_f32 v174, v162, v163
	v_pk_fma_f32 v[164:165], v[28:29], v[164:165], v[32:33]
	v_lshlrev_b32_e32 v167, 16, v166
	v_pk_fma_f32 v[164:165], v[156:157], v[164:165], v[160:161]
	v_sub_f32_e32 v167, v162, v167
	v_cvt_pk_bf16_f32 v168, v167, 0
	v_cvt_pk_bf16_f32 v167, v163, 0
	v_cvt_pk_bf16_f32 v172, v165, 0
	v_lshlrev_b32_e32 v167, 16, v167
	v_cvt_pk_bf16_f32 v170, v164, 0
	v_lshlrev_b32_e32 v172, 16, v172
	v_cvt_pk_fp8_f32 v174, v164, v165 op_sel:[0,0,1]
	v_sub_f32_e32 v169, v163, v167
	v_lshlrev_b32_e32 v171, 16, v170
	v_sub_f32_e32 v173, v165, v172
	v_cvt_pk_bf16_f32 v169, v169, 0
	v_sub_f32_e32 v171, v164, v171
	v_cvt_pk_bf16_f32 v173, v173, 0
	v_cvt_pk_bf16_f32 v171, v171, 0
	v_lshlrev_b32_e32 v162, 16, v169
	v_lshlrev_b32_e32 v163, 16, v173
	v_lshl_add_u64 v[164:165], s[12:13], 0, v[200:201]
	v_and_or_b32 v166, v166, s35, v167
	v_and_or_b32 v167, v170, s35, v172
	v_and_or_b32 v162, v168, s35, v162
	v_and_or_b32 v163, v171, s35, v163
	global_store_dword v[164:165], v174, off
	v_add_u32_e32 v164, s48, v237
	ds_write_b64 v164, v[166:167]
	ds_write_b64 v164, v[162:163] offset:33024
	s_waitcnt lgkmcnt(0)
	s_barrier
	ds_read_b128 v[162:165], v238
	ds_read_b128 v[166:169], v238 offset:64
	s_waitcnt lgkmcnt(1)
	v_mfma_f32_16x16x32_bf16 v[170:173], v[162:165], v[34:37], 0
	ds_read_b128 v[174:177], v238 offset:33024
	ds_read_b128 v[178:181], v238 offset:33088
	s_mov_b64 s[34:35], -1
	s_mov_b64 s[12:13], -1
	v_mfma_f32_16x16x32_bf16 v[182:185], v[162:165], v[42:45], 0
	s_waitcnt lgkmcnt(1)
	v_mfma_f32_16x16x32_bf16 v[170:173], v[174:177], v[34:37], v[170:173]
	v_mfma_f32_16x16x32_bf16 v[174:177], v[174:177], v[42:45], v[182:185]
	v_mfma_f32_16x16x32_bf16 v[170:173], v[162:165], v[38:41], v[170:173]
	v_mfma_f32_16x16x32_bf16 v[162:165], v[162:165], v[46:49], v[174:177]
	v_mfma_f32_16x16x32_bf16 v[170:173], v[166:169], v[50:53], v[170:173]
	v_mfma_f32_16x16x32_bf16 v[162:165], v[166:169], v[58:61], v[162:165]
	s_waitcnt lgkmcnt(0)
	v_mfma_f32_16x16x32_bf16 v[170:173], v[178:181], v[50:53], v[170:173]
	v_mfma_f32_16x16x32_bf16 v[162:165], v[178:181], v[58:61], v[162:165]
	v_mfma_f32_16x16x32_bf16 v[170:173], v[166:169], v[54:57], v[170:173]
	v_mfma_f32_16x16x32_bf16 v[162:165], v[166:169], v[62:65], v[162:165]
	ds_read_b128 v[166:169], v238 offset:128
	ds_read_b128 v[174:177], v238 offset:192
	ds_read_b128 v[178:181], v238 offset:33152
	ds_read_b128 v[182:185], v238 offset:33216
	s_waitcnt lgkmcnt(3)
	v_mfma_f32_16x16x32_bf16 v[170:173], v[166:169], v[66:69], v[170:173]
	v_mfma_f32_16x16x32_bf16 v[162:165], v[166:169], v[74:77], v[162:165]
	s_waitcnt lgkmcnt(1)
	v_mfma_f32_16x16x32_bf16 v[170:173], v[178:181], v[66:69], v[170:173]
	v_mfma_f32_16x16x32_bf16 v[162:165], v[178:181], v[74:77], v[162:165]
	v_mfma_f32_16x16x32_bf16 v[170:173], v[166:169], v[70:73], v[170:173]
	v_mfma_f32_16x16x32_bf16 v[162:165], v[166:169], v[78:81], v[162:165]
	v_mfma_f32_16x16x32_bf16 v[166:169], v[174:177], v[82:85], v[170:173]
	v_mfma_f32_16x16x32_bf16 v[162:165], v[174:177], v[90:93], v[162:165]
	s_waitcnt lgkmcnt(0)
	v_mfma_f32_16x16x32_bf16 v[166:169], v[182:185], v[82:85], v[166:169]
	v_mfma_f32_16x16x32_bf16 v[162:165], v[182:185], v[90:93], v[162:165]
	v_mfma_f32_16x16x32_bf16 v[166:169], v[174:177], v[86:89], v[166:169]
	v_mfma_f32_16x16x32_bf16 v[162:165], v[174:177], v[94:97], v[162:165]
	s_nop 7
	ds_write2_b32 v239, v166, v162 offset1:16
	ds_write2_b32 v239, v167, v163 offset0:32 offset1:48
	ds_write2_b32 v239, v168, v164 offset0:64 offset1:80
	ds_write2_b32 v239, v169, v165 offset0:96 offset1:112
	s_waitcnt lgkmcnt(0)
	s_barrier
	ds_read2st64_b32 v[162:163], v233 offset1:8
	ds_read2st64_b32 v[164:165], v233 offset0:16 offset1:24
	s_waitcnt vmcnt(0) lgkmcnt(1)
	v_add_f32_e32 v162, v242, v162
	ds_read2st64_b32 v[166:167], v233 offset0:32 offset1:40
	v_add_f32_e32 v168, v162, v163
	ds_read2st64_b32 v[162:163], v233 offset0:48 offset1:56
	s_waitcnt lgkmcnt(2)
	v_add_f32_e32 v164, v168, v164
	v_add_f32_e32 v164, v164, v165
	s_waitcnt lgkmcnt(1)
	v_add_f32_e32 v164, v164, v166
	v_add_f32_e32 v164, v164, v167
	s_waitcnt lgkmcnt(0)
	v_add_f32_e32 v162, v164, v162
	v_add_f32_e32 v165, v162, v163
	ds_bpermute_b32 v162, v230, v165
	ds_bpermute_b32 v163, v230, v232
	s_waitcnt lgkmcnt(1)
	v_cmp_nlt_f32_e32 vcc, v165, v162
	s_and_saveexec_b64 s[36:37], vcc
	s_cbranch_execz .LBB0_988
	v_cmp_eq_f32_e32 vcc, v165, v162
	s_waitcnt lgkmcnt(0)
	v_cmp_lt_i32_e64 s[12:13], v163, v232
	s_and_b64 s[12:13], vcc, s[12:13]
	s_orn2_b64 s[12:13], s[12:13], exec
